# v5 with expert counters 512 bytes apart (was 128)
# speedup vs baseline: 1.0006x; 1.0006x over previous
.LBB0_1059:
	s_or_b64 exec, exec, s[58:59]
	v_lshlrev_b32_e32 v98, 9, v98
	v_add_u32_e32 v98, 0xa000, v98
	v_mov_b32_e32 v99, 0
	v_lshl_add_u64 v[98:99], v[98:99], 0, s[26:27]
	global_atomic_add v106, v[98:99], v207, off sc0

.LBB0_1122:
	s_cmp_gt_i32 s28, 10
	s_cselect_b64 s[0:1], -1, 0
	s_cmp_lt_i32 s29, 11
	s_cselect_b64 s[6:7], -1, 0
	s_or_b64 s[0:1], s[0:1], s[6:7]
	s_and_b64 vcc, exec, s[0:1]
	s_cbranch_vccnz .LBB0_1244
	v_cmp_gt_u32_e32 vcc, 64, v0
	s_and_saveexec_b64 s[6:7], vcc
	s_cbranch_execz .LBB0_1127
	s_waitcnt vmcnt(0)
	v_and_b32_e32 v1, 31, v0
	s_waitcnt lgkmcnt(0)
	v_lshlrev_b32_e32 v2, 9, v1
	v_add_u32_e32 v2, 0xa000, v2
	global_load_dword v2, v2, s[26:27] sc1
	v_mbcnt_lo_u32_b32 v3, -1, 0
	v_mbcnt_hi_u32_b32 v4, -1, v3
	v_and_b32_e32 v5, 0x60, v4
	v_add_u32_e32 v3, -1, v4
	v_cmp_lt_i32_e32 vcc, v3, v5
	v_add_u32_e32 v6, -2, v4
	v_add_u32_e32 v7, -4, v4
	v_cndmask_b32_e32 v3, v3, v4, vcc
	v_lshlrev_b32_e32 v9, 2, v3
	v_cmp_lt_i32_e32 vcc, v6, v5
	v_add_u32_e32 v8, -8, v4
	s_waitcnt vmcnt(0)
	v_add_u32_e32 v3, 0xff, v2
	v_lshrrev_b32_e32 v3, 8, v3
	ds_bpermute_b32 v9, v9, v3
	v_cndmask_b32_e32 v6, v6, v4, vcc
	v_cmp_ne_u32_e32 vcc, 0, v1
	v_lshlrev_b32_e32 v6, 2, v6
	s_waitcnt lgkmcnt(0)
	v_cndmask_b32_e32 v9, 0, v9, vcc
	v_add_u32_e32 v9, v9, v3
	ds_bpermute_b32 v6, v6, v9
	v_cmp_lt_i32_e32 vcc, v7, v5
	s_nop 1
	v_cndmask_b32_e32 v7, v7, v4, vcc
	v_cmp_lt_u32_e32 vcc, 1, v1
	v_lshlrev_b32_e32 v7, 2, v7
	s_waitcnt lgkmcnt(0)
	v_cndmask_b32_e32 v6, 0, v6, vcc
	v_add_u32_e32 v6, v6, v9
	ds_bpermute_b32 v7, v7, v6
	v_cmp_lt_i32_e32 vcc, v8, v5
	s_nop 1
	v_cndmask_b32_e32 v8, v8, v4, vcc
	v_cmp_lt_u32_e32 vcc, 3, v1
	v_lshlrev_b32_e32 v8, 2, v8
	s_waitcnt lgkmcnt(0)
	v_cndmask_b32_e32 v7, 0, v7, vcc
	v_add_u32_e32 v6, v7, v6
	ds_bpermute_b32 v7, v8, v6
	v_add_u32_e32 v8, -16, v4
	v_cmp_lt_i32_e32 vcc, v8, v5
	s_nop 1
	v_cndmask_b32_e32 v5, v8, v4, vcc
	v_cmp_lt_u32_e32 vcc, 7, v1
	v_lshlrev_b32_e32 v5, 2, v5
	s_waitcnt lgkmcnt(0)
	v_cndmask_b32_e32 v4, 0, v7, vcc
	v_add_u32_e32 v4, v4, v6
	ds_bpermute_b32 v5, v5, v4
	v_cmp_gt_u32_e32 vcc, 32, v0
	s_and_b64 exec, exec, vcc
	s_cbranch_execz .LBB0_1127
	v_cmp_lt_u32_e32 vcc, 15, v1
	s_waitcnt lgkmcnt(0)
	s_nop 0
	v_cndmask_b32_e32 v5, 0, v5, vcc
	v_add_u32_e32 v4, v5, v4
	v_lshl_add_u32 v5, v1, 2, 0
	v_add_u32_e32 v5, 0x23c00, v5
	v_cmp_eq_u32_e32 vcc, 31, v1
	v_sub_u32_e32 v1, v4, v3
	ds_write2_b32 v5, v1, v2 offset1:33
	s_and_b64 exec, exec, vcc
	s_add_i32 s3, 0, 0x23c80
	v_mov_b32_e32 v1, s3
	ds_write_b32 v1, v4

.LBB0_1244:
	s_cmp_lt_i32 s28, 12
	s_cselect_b64 s[6:7], -1, 0
	s_cmp_gt_i32 s29, 11
	s_cselect_b64 s[8:9], -1, 0
	s_and_b64 s[6:7], s[6:7], s[8:9]
	s_andn2_b64 vcc, exec, s[6:7]
	s_cbranch_vccnz .LBB0_1368
	s_andn2_b64 vcc, exec, s[0:1]
	s_cbranch_vccnz .LBB0_1251
	v_cmp_gt_u32_e32 vcc, 64, v0
	s_and_saveexec_b64 s[6:7], vcc
	s_cbranch_execz .LBB0_1250
	s_waitcnt vmcnt(0)
	v_and_b32_e32 v1, 31, v0
	s_waitcnt lgkmcnt(0)
	v_lshlrev_b32_e32 v2, 9, v1
	v_add_u32_e32 v2, 0xa000, v2
	global_load_dword v2, v2, s[26:27] sc1
	v_mbcnt_lo_u32_b32 v3, -1, 0
	v_mbcnt_hi_u32_b32 v4, -1, v3
	v_and_b32_e32 v5, 0x60, v4
	v_add_u32_e32 v3, -1, v4
	v_cmp_lt_i32_e32 vcc, v3, v5
	v_add_u32_e32 v6, -2, v4
	v_add_u32_e32 v7, -4, v4
	v_cndmask_b32_e32 v3, v3, v4, vcc
	v_lshlrev_b32_e32 v9, 2, v3
	v_cmp_lt_i32_e32 vcc, v6, v5
	v_add_u32_e32 v8, -8, v4
	s_waitcnt vmcnt(0)
	v_add_u32_e32 v3, 0xff, v2
	v_lshrrev_b32_e32 v3, 8, v3
	ds_bpermute_b32 v9, v9, v3
	v_cndmask_b32_e32 v6, v6, v4, vcc
	v_cmp_ne_u32_e32 vcc, 0, v1
	v_lshlrev_b32_e32 v6, 2, v6
	s_waitcnt lgkmcnt(0)
	v_cndmask_b32_e32 v9, 0, v9, vcc
	v_add_u32_e32 v9, v9, v3
	ds_bpermute_b32 v6, v6, v9
	v_cmp_lt_i32_e32 vcc, v7, v5
	s_nop 1
	v_cndmask_b32_e32 v7, v7, v4, vcc
	v_cmp_lt_u32_e32 vcc, 1, v1
	v_lshlrev_b32_e32 v7, 2, v7
	s_waitcnt lgkmcnt(0)
	v_cndmask_b32_e32 v6, 0, v6, vcc
	v_add_u32_e32 v6, v6, v9
	ds_bpermute_b32 v7, v7, v6
	v_cmp_lt_i32_e32 vcc, v8, v5
	s_nop 1
	v_cndmask_b32_e32 v8, v8, v4, vcc
	v_cmp_lt_u32_e32 vcc, 3, v1
	v_lshlrev_b32_e32 v8, 2, v8
	s_waitcnt lgkmcnt(0)
	v_cndmask_b32_e32 v7, 0, v7, vcc
	v_add_u32_e32 v6, v7, v6
	ds_bpermute_b32 v7, v8, v6
	v_add_u32_e32 v8, -16, v4
	v_cmp_lt_i32_e32 vcc, v8, v5
	s_nop 1
	v_cndmask_b32_e32 v5, v8, v4, vcc
	v_cmp_lt_u32_e32 vcc, 7, v1
	v_lshlrev_b32_e32 v5, 2, v5
	s_waitcnt lgkmcnt(0)
	v_cndmask_b32_e32 v4, 0, v7, vcc
	v_add_u32_e32 v4, v4, v6
	ds_bpermute_b32 v5, v5, v4
	v_cmp_gt_u32_e32 vcc, 32, v0
	s_and_b64 exec, exec, vcc
	s_cbranch_execz .LBB0_1250
	v_cmp_lt_u32_e32 vcc, 15, v1
	s_waitcnt lgkmcnt(0)
	s_nop 0
	v_cndmask_b32_e32 v5, 0, v5, vcc
	v_add_u32_e32 v4, v5, v4
	v_lshl_add_u32 v5, v1, 2, 0
	v_add_u32_e32 v5, 0x23c00, v5
	v_cmp_eq_u32_e32 vcc, 31, v1
	v_sub_u32_e32 v1, v4, v3
	ds_write2_b32 v5, v1, v2 offset1:33
	s_and_b64 exec, exec, vcc
	s_add_i32 s3, 0, 0x23c80
	v_mov_b32_e32 v1, s3
	ds_write_b32 v1, v4

.LBB0_1368:
	s_cmp_lt_i32 s28, 13
	s_cselect_b64 s[4:5], -1, 0
	s_cmp_gt_i32 s29, 12
	s_cselect_b64 s[6:7], -1, 0
	s_and_b64 s[4:5], s[4:5], s[6:7]
	s_andn2_b64 vcc, exec, s[4:5]
	s_cbranch_vccnz .LBB0_1380
	s_andn2_b64 vcc, exec, s[0:1]
	s_cbranch_vccnz .LBB0_1375
	v_cmp_gt_u32_e32 vcc, 64, v0
	s_and_saveexec_b64 s[0:1], vcc
	s_cbranch_execz .LBB0_1374
	s_waitcnt vmcnt(0)
	v_and_b32_e32 v1, 31, v0
	s_waitcnt lgkmcnt(0)
	v_lshlrev_b32_e32 v2, 9, v1
	v_add_u32_e32 v2, 0xa000, v2
	global_load_dword v2, v2, s[26:27] sc1
	v_mbcnt_lo_u32_b32 v3, -1, 0
	v_mbcnt_hi_u32_b32 v4, -1, v3
	v_and_b32_e32 v5, 0x60, v4
	v_add_u32_e32 v3, -1, v4
	v_cmp_lt_i32_e32 vcc, v3, v5
	v_add_u32_e32 v6, -2, v4
	v_add_u32_e32 v7, -4, v4
	v_cndmask_b32_e32 v3, v3, v4, vcc
	v_lshlrev_b32_e32 v9, 2, v3
	v_cmp_lt_i32_e32 vcc, v6, v5
	v_add_u32_e32 v8, -8, v4
	s_waitcnt vmcnt(0)
	v_add_u32_e32 v3, 0xff, v2
	v_lshrrev_b32_e32 v3, 8, v3
	ds_bpermute_b32 v9, v9, v3
	v_cndmask_b32_e32 v6, v6, v4, vcc
	v_cmp_ne_u32_e32 vcc, 0, v1
	v_lshlrev_b32_e32 v6, 2, v6
	s_waitcnt lgkmcnt(0)
	v_cndmask_b32_e32 v9, 0, v9, vcc
	v_add_u32_e32 v9, v9, v3
	ds_bpermute_b32 v6, v6, v9
	v_cmp_lt_i32_e32 vcc, v7, v5
	s_nop 1
	v_cndmask_b32_e32 v7, v7, v4, vcc
	v_cmp_lt_u32_e32 vcc, 1, v1
	v_lshlrev_b32_e32 v7, 2, v7
	s_waitcnt lgkmcnt(0)
	v_cndmask_b32_e32 v6, 0, v6, vcc
	v_add_u32_e32 v6, v6, v9
	ds_bpermute_b32 v7, v7, v6
	v_cmp_lt_i32_e32 vcc, v8, v5
	s_nop 1
	v_cndmask_b32_e32 v8, v8, v4, vcc
	v_cmp_lt_u32_e32 vcc, 3, v1
	v_lshlrev_b32_e32 v8, 2, v8
	s_waitcnt lgkmcnt(0)
	v_cndmask_b32_e32 v7, 0, v7, vcc
	v_add_u32_e32 v6, v7, v6
	ds_bpermute_b32 v7, v8, v6
	v_add_u32_e32 v8, -16, v4
	v_cmp_lt_i32_e32 vcc, v8, v5
	s_nop 1
	v_cndmask_b32_e32 v5, v8, v4, vcc
	v_cmp_lt_u32_e32 vcc, 7, v1
	v_lshlrev_b32_e32 v5, 2, v5
	s_waitcnt lgkmcnt(0)
	v_cndmask_b32_e32 v4, 0, v7, vcc
	v_add_u32_e32 v4, v4, v6
	ds_bpermute_b32 v5, v5, v4
	v_cmp_gt_u32_e32 vcc, 32, v0
	s_and_b64 exec, exec, vcc
	s_cbranch_execz .LBB0_1374
	v_cmp_lt_u32_e32 vcc, 15, v1
	s_waitcnt lgkmcnt(0)
	s_nop 0
	v_cndmask_b32_e32 v0, 0, v5, vcc
	v_add_u32_e32 v0, v0, v4
	v_lshl_add_u32 v4, v1, 2, 0
	v_add_u32_e32 v4, 0x23c00, v4
	v_cmp_eq_u32_e32 vcc, 31, v1
	v_sub_u32_e32 v1, v0, v3
	ds_write2_b32 v4, v1, v2 offset1:33
	s_and_b64 exec, exec, vcc
	s_add_i32 s3, 0, 0x23c80
	v_mov_b32_e32 v1, s3
	ds_write_b32 v1, v0
